# scan wave rescheduled: next step's state conversions, decay multiplies and operand loads issued in the issue stalls of the current step's four f32 MFMAs
# baseline (speedup 1.0000x reference)
; #define LAS __attribute__((address_space(3)))
; __device__ __forceinline__ void scan_head(const Params& p, LAS unsigned char* lds, int bh, const int wave) {
;     ...
;             __builtin_amdgcn_s_setprio(3);
;             const int bp = chunk & 1, vb = chunk % 3;
;             const LAS unsigned char* awp = lds + L_AW + bp * 8192 + sel * 128 + rg * 16;
;             const LAS unsigned char* wwp = lds + L_W + bp * 8192 + rg * 16;
;             const LAS unsigned char* abp = lds + L_BK + bp * 16384 + rg * 256 + ri * 4;
;             const LAS unsigned char* vp = lds + L_V + vb * 8192 + (16 * wave + ri) * 4;
;             const LAS unsigned char* csp = lds + L_CS + bp * 256;
;             LAS unsigned char* yp = (rg == 0) ? (lds + L_Y + bp * 8192 + (16 * wave + ri) * 4) : ((rg == 2) ? (lds + L_Y + bp * 8192 + 256 + (16 * wave + ri) * 4) : (lds + L_DUMMY + tid * 4));
;             const int y_st = (rg & 1) ? 0 : 512;
;     ...
;             bf16x8 Pa0, Pa1, Qa0, Qa1; f32x4 Pw0, Pw1, Pw2, Pw3, Qw0, Qw1, Qw2, Qw3, Pcs, Qcs; float Pb0, Pb1, Pb2, Pb3, Pvt, Pvu, Qb0, Qb1, Qb2, Qb3, Qvt, Qvu;
;             SCAN_LD(P, 0);
; #pragma unroll 1
;             for (int pi = 0; pi < 16; pi += 2) {
;                 SCAN_LD(Q, pi + 1);
;                 SCAN_STEP(P, pi);
;                 if (pi + 2 < 16) SCAN_LD(P, pi + 2);
;                 SCAN_STEP(Q, pi + 1);
;             }
.LBB0_806:
	s_and_b64 vcc, exec, s[14:15]
	s_cbranch_vccz .LBB0_789
	s_setprio 3
	s_and_b32 s2, s51, 1
	s_lshl_b32 s15, s2, 13
	s_mul_i32 s14, s51, 0xab
	s_lshl_b32 s52, s2, 14
	s_bfe_u32 s14, s14, 0x70009
	s_lshl_b32 s44, s2, 8
	s_mul_i32 s14, s14, 3
	s_waitcnt vmcnt(0)
	s_sub_i32 s14, s51, s14
	s_and_b32 s14, s14, 0xff
	s_lshl_b32 s14, s14, 13
	s_add_i32 s44, s44, 0x20300
	v_add_u32_e32 v98, s15, v176
	v_add_u32_e32 v99, s15, v175
	v_add_u32_e32 v0, s52, v178
	v_add_u32_e32 v1, s14, v179
	v_add_u32_e32 v0, 0x8000, v0
	v_add_u32_e32 v4, 0x100, v1
	v_mov_b32_e32 v2, s44
	v_cndmask_b32_e64 v4, v4, v1, s[8:9]
	v_cndmask_b32_e64 v4, v4, v1, s[12:13]
	v_cndmask_b32_e64 v1, v4, v1, s[10:11]
	v_add_u32_e32 v4, s15, v181
	v_add_u32_e32 v6, 0xd00, v180
	v_add_u32_e32 v5, 0x100, v4
	v_cndmask_b32_e64 v5, v6, v5, s[10:11]
	v_cndmask_b32_e64 v3, v5, v4, s[8:9]
	ds_read_b128 v[68:71], v98 offset:0
	ds_read_b128 v[72:75], v98 offset:64
	ds_read_b128 v[76:79], v99 offset:16384
	ds_read_b128 v[80:83], v99 offset:16448
	ds_read_b128 v[84:87], v99 offset:16512
	ds_read_b128 v[88:91], v99 offset:16576
	ds_read2_b32 v[92:93], v0 offset1:16
	ds_read2_b32 v[94:95], v0 offset0:32 offset1:48
	ds_read_b32 v96, v1 offset:0
	ds_read_b128 v[100:103], v2 offset:0
	v_cvt_pk_bf16_f32 v8, v64, v65
	v_cvt_pk_bf16_f32 v9, v66, v67
	v_cvt_pk_bf16_f32 v10, v60, v61
	v_cvt_pk_bf16_f32 v11, v62, v63
	s_waitcnt lgkmcnt(5)
	v_pk_mul_f32 v[64:65], v[64:65], v[76:77]
	v_pk_mul_f32 v[66:67], v[66:67], v[78:79]
	v_pk_mul_f32 v[60:61], v[60:61], v[80:81]
	v_pk_mul_f32 v[62:63], v[62:63], v[82:83]
	v_mfma_f32_16x16x32_bf16 v[140:143], v[68:71], v[8:11], 0
	v_cvt_pk_bf16_f32 v12, v52, v53
	v_cvt_pk_bf16_f32 v13, v54, v55
	v_cvt_pk_bf16_f32 v14, v56, v57
	v_cvt_pk_bf16_f32 v15, v58, v59
	v_pk_mul_f32 v[52:53], v[52:53], v[84:85]
	v_pk_mul_f32 v[54:55], v[54:55], v[86:87]
	v_mfma_f32_16x16x32_bf16 v[140:143], v[72:75], v[12:15], v[140:143]
	s_waitcnt lgkmcnt(4)
	v_pk_mul_f32 v[56:57], v[56:57], v[88:89]
	v_pk_mul_f32 v[58:59], v[58:59], v[90:91]
	ds_read_b128 v[104:107], v98 offset:512
	ds_read_b128 v[108:111], v98 offset:576
	ds_read_b128 v[112:115], v99 offset:16640
	ds_read_b128 v[116:119], v99 offset:16704
	ds_read_b128 v[120:123], v99 offset:16768
	s_waitcnt lgkmcnt(5)
	v_fma_f32 v144, v100, v140, v142
	v_fmac_f32_e32 v144, v101, v96
	v_cndmask_b32_e64 v145, v96, v144, s[10:11]
	v_cndmask_b32_e64 v145, v145, v140, s[8:9]
	v_fma_f32 v50, v102, v140, v143
	v_fmac_f32_e32 v50, v103, v96
	v_mfma_f32_16x16x4_f32 v[64:67], v92, v145, v[64:67]
	ds_read_b128 v[128:131], v99 offset:16832
	v_add_u32_e32 v0, 0x400, v0
	ds_read2_b32 v[132:133], v0 offset1:16
	ds_read2_b32 v[134:135], v0 offset0:32 offset1:48
	v_mfma_f32_16x16x4_f32 v[60:63], v93, v145, v[60:63]
	ds_read_b32 v97, v1 offset:512
	ds_read_b128 v[136:139], v2 offset:16
	v_cndmask_b32_e64 v50, v50, v141, s[8:9]
	ds_write_b32 v3, v50 offset:0
	v_mfma_f32_16x16x4_f32 v[52:55], v94, v145, v[52:55]
	v_cvt_pk_bf16_f32 v8, v64, v65
	v_cvt_pk_bf16_f32 v9, v66, v67
	v_mfma_f32_16x16x4_f32 v[56:59], v95, v145, v[56:59]
	s_waitcnt lgkmcnt(6)
	v_pk_mul_f32 v[64:65], v[64:65], v[112:113]
	v_pk_mul_f32 v[66:67], v[66:67], v[114:115]
	v_cvt_pk_bf16_f32 v10, v60, v61
	v_cvt_pk_bf16_f32 v11, v62, v63
	v_pk_mul_f32 v[60:61], v[60:61], v[116:117]
	v_pk_mul_f32 v[62:63], v[62:63], v[118:119]
	v_mfma_f32_16x16x32_bf16 v[140:143], v[104:107], v[8:11], 0
	v_cvt_pk_bf16_f32 v12, v52, v53
	v_cvt_pk_bf16_f32 v13, v54, v55
	v_cvt_pk_bf16_f32 v14, v56, v57
	v_cvt_pk_bf16_f32 v15, v58, v59
	v_pk_mul_f32 v[52:53], v[52:53], v[120:121]
	v_pk_mul_f32 v[54:55], v[54:55], v[122:123]
	v_mfma_f32_16x16x32_bf16 v[140:143], v[108:111], v[12:15], v[140:143]
	s_waitcnt lgkmcnt(5)
	v_pk_mul_f32 v[56:57], v[56:57], v[128:129]
	v_pk_mul_f32 v[58:59], v[58:59], v[130:131]
	ds_read_b128 v[68:71], v98 offset:1024
	ds_read_b128 v[72:75], v98 offset:1088
	ds_read_b128 v[76:79], v99 offset:16896
	ds_read_b128 v[80:83], v99 offset:16960
	ds_read_b128 v[84:87], v99 offset:17024
	s_waitcnt lgkmcnt(6)
	v_fma_f32 v144, v136, v140, v142
	v_fmac_f32_e32 v144, v137, v97
	v_cndmask_b32_e64 v145, v97, v144, s[10:11]
	v_cndmask_b32_e64 v145, v145, v140, s[8:9]
	v_fma_f32 v50, v138, v140, v143
	v_fmac_f32_e32 v50, v139, v97
	v_mfma_f32_16x16x4_f32 v[64:67], v132, v145, v[64:67]
	ds_read_b128 v[88:91], v99 offset:17088
	v_add_u32_e32 v0, 0x400, v0
	ds_read2_b32 v[92:93], v0 offset1:16
	ds_read2_b32 v[94:95], v0 offset0:32 offset1:48
	v_mfma_f32_16x16x4_f32 v[60:63], v133, v145, v[60:63]
	ds_read_b32 v96, v1 offset:1024
	ds_read_b128 v[100:103], v2 offset:32
	v_cndmask_b32_e64 v50, v50, v141, s[8:9]
	ds_write_b32 v3, v50 offset:512
	v_mfma_f32_16x16x4_f32 v[52:55], v134, v145, v[52:55]
	v_cvt_pk_bf16_f32 v8, v64, v65
	v_cvt_pk_bf16_f32 v9, v66, v67
	v_mfma_f32_16x16x4_f32 v[56:59], v135, v145, v[56:59]
	s_waitcnt lgkmcnt(6)
	v_pk_mul_f32 v[64:65], v[64:65], v[76:77]
	v_pk_mul_f32 v[66:67], v[66:67], v[78:79]
	v_cvt_pk_bf16_f32 v10, v60, v61
	v_cvt_pk_bf16_f32 v11, v62, v63
	v_pk_mul_f32 v[60:61], v[60:61], v[80:81]
	v_pk_mul_f32 v[62:63], v[62:63], v[82:83]
	v_mfma_f32_16x16x32_bf16 v[140:143], v[68:71], v[8:11], 0
	v_cvt_pk_bf16_f32 v12, v52, v53
	v_cvt_pk_bf16_f32 v13, v54, v55
	v_cvt_pk_bf16_f32 v14, v56, v57
	v_cvt_pk_bf16_f32 v15, v58, v59
	v_pk_mul_f32 v[52:53], v[52:53], v[84:85]
	v_pk_mul_f32 v[54:55], v[54:55], v[86:87]
	v_mfma_f32_16x16x32_bf16 v[140:143], v[72:75], v[12:15], v[140:143]
	s_waitcnt lgkmcnt(5)
	v_pk_mul_f32 v[56:57], v[56:57], v[88:89]
	v_pk_mul_f32 v[58:59], v[58:59], v[90:91]
	ds_read_b128 v[104:107], v98 offset:1536
	ds_read_b128 v[108:111], v98 offset:1600
	ds_read_b128 v[112:115], v99 offset:17152
	ds_read_b128 v[116:119], v99 offset:17216
	ds_read_b128 v[120:123], v99 offset:17280
	s_waitcnt lgkmcnt(6)
; __device__ __forceinline__ void scan_head(const Params& p, LAS unsigned char* lds, int bh, const int wave) {
;     ...
;             bf16x8 Pa0, Pa1, Qa0, Qa1; f32x4 Pw0, Pw1, Pw2, Pw3, Qw0, Qw1, Qw2, Qw3, Pcs, Qcs; float Pb0, Pb1, Pb2, Pb3, Pvt, Pvu, Qb0, Qb1, Qb2, Qb3, Qvt, Qvu;
;             SCAN_LD(P, 0);
; #pragma unroll 1
;             for (int pi = 0; pi < 16; pi += 2) {
;                 SCAN_LD(Q, pi + 1);
;                 SCAN_STEP(P, pi);
;                 if (pi + 2 < 16) SCAN_LD(P, pi + 2);
;                 SCAN_STEP(Q, pi + 1);
;             }
	v_fma_f32 v144, v100, v140, v142
	v_fmac_f32_e32 v144, v101, v96
	v_cndmask_b32_e64 v145, v96, v144, s[10:11]
	v_cndmask_b32_e64 v145, v145, v140, s[8:9]
	v_fma_f32 v50, v102, v140, v143
	v_fmac_f32_e32 v50, v103, v96
	v_mfma_f32_16x16x4_f32 v[64:67], v92, v145, v[64:67]
	ds_read_b128 v[128:131], v99 offset:17344
	v_add_u32_e32 v0, 0x400, v0
	ds_read2_b32 v[132:133], v0 offset1:16
	ds_read2_b32 v[134:135], v0 offset0:32 offset1:48
	v_mfma_f32_16x16x4_f32 v[60:63], v93, v145, v[60:63]
	ds_read_b32 v97, v1 offset:1536
	ds_read_b128 v[136:139], v2 offset:48
	v_cndmask_b32_e64 v50, v50, v141, s[8:9]
	ds_write_b32 v3, v50 offset:1024
	v_mfma_f32_16x16x4_f32 v[52:55], v94, v145, v[52:55]
	v_cvt_pk_bf16_f32 v8, v64, v65
	v_cvt_pk_bf16_f32 v9, v66, v67
	v_mfma_f32_16x16x4_f32 v[56:59], v95, v145, v[56:59]
	s_waitcnt lgkmcnt(6)
	v_pk_mul_f32 v[64:65], v[64:65], v[112:113]
	v_pk_mul_f32 v[66:67], v[66:67], v[114:115]
	v_cvt_pk_bf16_f32 v10, v60, v61
	v_cvt_pk_bf16_f32 v11, v62, v63
	v_pk_mul_f32 v[60:61], v[60:61], v[116:117]
	v_pk_mul_f32 v[62:63], v[62:63], v[118:119]
	v_mfma_f32_16x16x32_bf16 v[140:143], v[104:107], v[8:11], 0
	v_cvt_pk_bf16_f32 v12, v52, v53
	v_cvt_pk_bf16_f32 v13, v54, v55
	v_cvt_pk_bf16_f32 v14, v56, v57
	v_cvt_pk_bf16_f32 v15, v58, v59
	v_pk_mul_f32 v[52:53], v[52:53], v[120:121]
	v_pk_mul_f32 v[54:55], v[54:55], v[122:123]
	v_mfma_f32_16x16x32_bf16 v[140:143], v[108:111], v[12:15], v[140:143]
	s_waitcnt lgkmcnt(5)
	v_pk_mul_f32 v[56:57], v[56:57], v[128:129]
	v_pk_mul_f32 v[58:59], v[58:59], v[130:131]
	ds_read_b128 v[68:71], v98 offset:2048
	ds_read_b128 v[72:75], v98 offset:2112
	ds_read_b128 v[76:79], v99 offset:17408
	ds_read_b128 v[80:83], v99 offset:17472
	ds_read_b128 v[84:87], v99 offset:17536
	s_waitcnt lgkmcnt(6)
	v_fma_f32 v144, v136, v140, v142
	v_fmac_f32_e32 v144, v137, v97
	v_cndmask_b32_e64 v145, v97, v144, s[10:11]
	v_cndmask_b32_e64 v145, v145, v140, s[8:9]
	v_fma_f32 v50, v138, v140, v143
	v_fmac_f32_e32 v50, v139, v97
	v_mfma_f32_16x16x4_f32 v[64:67], v132, v145, v[64:67]
	ds_read_b128 v[88:91], v99 offset:17600
	v_add_u32_e32 v0, 0x400, v0
	ds_read2_b32 v[92:93], v0 offset1:16
	ds_read2_b32 v[94:95], v0 offset0:32 offset1:48
	v_mfma_f32_16x16x4_f32 v[60:63], v133, v145, v[60:63]
	ds_read_b32 v96, v1 offset:2048
	ds_read_b128 v[100:103], v2 offset:64
	v_cndmask_b32_e64 v50, v50, v141, s[8:9]
	ds_write_b32 v3, v50 offset:1536
	v_mfma_f32_16x16x4_f32 v[52:55], v134, v145, v[52:55]
	v_cvt_pk_bf16_f32 v8, v64, v65
	v_cvt_pk_bf16_f32 v9, v66, v67
	v_mfma_f32_16x16x4_f32 v[56:59], v135, v145, v[56:59]
	s_waitcnt lgkmcnt(6)
	v_pk_mul_f32 v[64:65], v[64:65], v[76:77]
	v_pk_mul_f32 v[66:67], v[66:67], v[78:79]
	v_cvt_pk_bf16_f32 v10, v60, v61
	v_cvt_pk_bf16_f32 v11, v62, v63
	v_pk_mul_f32 v[60:61], v[60:61], v[80:81]
	v_pk_mul_f32 v[62:63], v[62:63], v[82:83]
	v_mfma_f32_16x16x32_bf16 v[140:143], v[68:71], v[8:11], 0
	v_cvt_pk_bf16_f32 v12, v52, v53
	v_cvt_pk_bf16_f32 v13, v54, v55
	v_cvt_pk_bf16_f32 v14, v56, v57
	v_cvt_pk_bf16_f32 v15, v58, v59
	v_pk_mul_f32 v[52:53], v[52:53], v[84:85]
	v_pk_mul_f32 v[54:55], v[54:55], v[86:87]
	v_mfma_f32_16x16x32_bf16 v[140:143], v[72:75], v[12:15], v[140:143]
	s_waitcnt lgkmcnt(5)
	v_pk_mul_f32 v[56:57], v[56:57], v[88:89]
	v_pk_mul_f32 v[58:59], v[58:59], v[90:91]
	ds_read_b128 v[104:107], v98 offset:2560
	ds_read_b128 v[108:111], v98 offset:2624
	ds_read_b128 v[112:115], v99 offset:17664
	ds_read_b128 v[116:119], v99 offset:17728
	ds_read_b128 v[120:123], v99 offset:17792
	s_waitcnt lgkmcnt(6)
	v_fma_f32 v144, v100, v140, v142
	v_fmac_f32_e32 v144, v101, v96
	v_cndmask_b32_e64 v145, v96, v144, s[10:11]
	v_cndmask_b32_e64 v145, v145, v140, s[8:9]
	v_fma_f32 v50, v102, v140, v143
	v_fmac_f32_e32 v50, v103, v96
	v_mfma_f32_16x16x4_f32 v[64:67], v92, v145, v[64:67]
	ds_read_b128 v[128:131], v99 offset:17856
	v_add_u32_e32 v0, 0x400, v0
	ds_read2_b32 v[132:133], v0 offset1:16
	ds_read2_b32 v[134:135], v0 offset0:32 offset1:48
	v_mfma_f32_16x16x4_f32 v[60:63], v93, v145, v[60:63]
	ds_read_b32 v97, v1 offset:2560
	ds_read_b128 v[136:139], v2 offset:80
	v_cndmask_b32_e64 v50, v50, v141, s[8:9]
	ds_write_b32 v3, v50 offset:2048
	v_mfma_f32_16x16x4_f32 v[52:55], v94, v145, v[52:55]
	v_cvt_pk_bf16_f32 v8, v64, v65
	v_cvt_pk_bf16_f32 v9, v66, v67
	v_mfma_f32_16x16x4_f32 v[56:59], v95, v145, v[56:59]
	s_waitcnt lgkmcnt(6)
	v_pk_mul_f32 v[64:65], v[64:65], v[112:113]
	v_pk_mul_f32 v[66:67], v[66:67], v[114:115]
	v_cvt_pk_bf16_f32 v10, v60, v61
	v_cvt_pk_bf16_f32 v11, v62, v63
	v_pk_mul_f32 v[60:61], v[60:61], v[116:117]
	v_pk_mul_f32 v[62:63], v[62:63], v[118:119]
	v_mfma_f32_16x16x32_bf16 v[140:143], v[104:107], v[8:11], 0
	v_cvt_pk_bf16_f32 v12, v52, v53
	v_cvt_pk_bf16_f32 v13, v54, v55
	v_cvt_pk_bf16_f32 v14, v56, v57
	v_cvt_pk_bf16_f32 v15, v58, v59
	v_pk_mul_f32 v[52:53], v[52:53], v[120:121]
	v_pk_mul_f32 v[54:55], v[54:55], v[122:123]
	v_mfma_f32_16x16x32_bf16 v[140:143], v[108:111], v[12:15], v[140:143]
	s_waitcnt lgkmcnt(5)
	v_pk_mul_f32 v[56:57], v[56:57], v[128:129]
	v_pk_mul_f32 v[58:59], v[58:59], v[130:131]
	ds_read_b128 v[68:71], v98 offset:3072
	ds_read_b128 v[72:75], v98 offset:3136
	ds_read_b128 v[76:79], v99 offset:17920
	ds_read_b128 v[80:83], v99 offset:17984
	ds_read_b128 v[84:87], v99 offset:18048
	s_waitcnt lgkmcnt(6)
; __device__ __forceinline__ void scan_head(const Params& p, LAS unsigned char* lds, int bh, const int wave) {
;     ...
;             bf16x8 Pa0, Pa1, Qa0, Qa1; f32x4 Pw0, Pw1, Pw2, Pw3, Qw0, Qw1, Qw2, Qw3, Pcs, Qcs; float Pb0, Pb1, Pb2, Pb3, Pvt, Pvu, Qb0, Qb1, Qb2, Qb3, Qvt, Qvu;
;             SCAN_LD(P, 0);
; #pragma unroll 1
;             for (int pi = 0; pi < 16; pi += 2) {
;                 SCAN_LD(Q, pi + 1);
;                 SCAN_STEP(P, pi);
;                 if (pi + 2 < 16) SCAN_LD(P, pi + 2);
;                 SCAN_STEP(Q, pi + 1);
;             }
	v_fma_f32 v144, v136, v140, v142
	v_fmac_f32_e32 v144, v137, v97
	v_cndmask_b32_e64 v145, v97, v144, s[10:11]
	v_cndmask_b32_e64 v145, v145, v140, s[8:9]
	v_fma_f32 v50, v138, v140, v143
	v_fmac_f32_e32 v50, v139, v97
	v_mfma_f32_16x16x4_f32 v[64:67], v132, v145, v[64:67]
	ds_read_b128 v[88:91], v99 offset:18112
	v_add_u32_e32 v0, 0x400, v0
	ds_read2_b32 v[92:93], v0 offset1:16
	ds_read2_b32 v[94:95], v0 offset0:32 offset1:48
	v_mfma_f32_16x16x4_f32 v[60:63], v133, v145, v[60:63]
	ds_read_b32 v96, v1 offset:3072
	ds_read_b128 v[100:103], v2 offset:96
	v_cndmask_b32_e64 v50, v50, v141, s[8:9]
	ds_write_b32 v3, v50 offset:2560
	v_mfma_f32_16x16x4_f32 v[52:55], v134, v145, v[52:55]
	v_cvt_pk_bf16_f32 v8, v64, v65
	v_cvt_pk_bf16_f32 v9, v66, v67
	v_mfma_f32_16x16x4_f32 v[56:59], v135, v145, v[56:59]
	s_waitcnt lgkmcnt(6)
	v_pk_mul_f32 v[64:65], v[64:65], v[76:77]
	v_pk_mul_f32 v[66:67], v[66:67], v[78:79]
	v_cvt_pk_bf16_f32 v10, v60, v61
	v_cvt_pk_bf16_f32 v11, v62, v63
	v_pk_mul_f32 v[60:61], v[60:61], v[80:81]
	v_pk_mul_f32 v[62:63], v[62:63], v[82:83]
	v_mfma_f32_16x16x32_bf16 v[140:143], v[68:71], v[8:11], 0
	v_cvt_pk_bf16_f32 v12, v52, v53
	v_cvt_pk_bf16_f32 v13, v54, v55
	v_cvt_pk_bf16_f32 v14, v56, v57
	v_cvt_pk_bf16_f32 v15, v58, v59
	v_pk_mul_f32 v[52:53], v[52:53], v[84:85]
	v_pk_mul_f32 v[54:55], v[54:55], v[86:87]
	v_mfma_f32_16x16x32_bf16 v[140:143], v[72:75], v[12:15], v[140:143]
	s_waitcnt lgkmcnt(5)
	v_pk_mul_f32 v[56:57], v[56:57], v[88:89]
	v_pk_mul_f32 v[58:59], v[58:59], v[90:91]
	ds_read_b128 v[104:107], v98 offset:3584
	ds_read_b128 v[108:111], v98 offset:3648
	ds_read_b128 v[112:115], v99 offset:18176
	ds_read_b128 v[116:119], v99 offset:18240
	ds_read_b128 v[120:123], v99 offset:18304
	s_waitcnt lgkmcnt(6)
	v_fma_f32 v144, v100, v140, v142
	v_fmac_f32_e32 v144, v101, v96
	v_cndmask_b32_e64 v145, v96, v144, s[10:11]
	v_cndmask_b32_e64 v145, v145, v140, s[8:9]
	v_fma_f32 v50, v102, v140, v143
	v_fmac_f32_e32 v50, v103, v96
	v_mfma_f32_16x16x4_f32 v[64:67], v92, v145, v[64:67]
	ds_read_b128 v[128:131], v99 offset:18368
	v_add_u32_e32 v0, 0x400, v0
	ds_read2_b32 v[132:133], v0 offset1:16
	ds_read2_b32 v[134:135], v0 offset0:32 offset1:48
	v_mfma_f32_16x16x4_f32 v[60:63], v93, v145, v[60:63]
	ds_read_b32 v97, v1 offset:3584
	ds_read_b128 v[136:139], v2 offset:112
	v_cndmask_b32_e64 v50, v50, v141, s[8:9]
	ds_write_b32 v3, v50 offset:3072
	v_mfma_f32_16x16x4_f32 v[52:55], v94, v145, v[52:55]
	v_cvt_pk_bf16_f32 v8, v64, v65
	v_cvt_pk_bf16_f32 v9, v66, v67
	v_mfma_f32_16x16x4_f32 v[56:59], v95, v145, v[56:59]
	s_waitcnt lgkmcnt(6)
	v_pk_mul_f32 v[64:65], v[64:65], v[112:113]
	v_pk_mul_f32 v[66:67], v[66:67], v[114:115]
	v_cvt_pk_bf16_f32 v10, v60, v61
	v_cvt_pk_bf16_f32 v11, v62, v63
	v_pk_mul_f32 v[60:61], v[60:61], v[116:117]
	v_pk_mul_f32 v[62:63], v[62:63], v[118:119]
	v_mfma_f32_16x16x32_bf16 v[140:143], v[104:107], v[8:11], 0
	v_cvt_pk_bf16_f32 v12, v52, v53
	v_cvt_pk_bf16_f32 v13, v54, v55
	v_cvt_pk_bf16_f32 v14, v56, v57
	v_cvt_pk_bf16_f32 v15, v58, v59
	v_pk_mul_f32 v[52:53], v[52:53], v[120:121]
	v_pk_mul_f32 v[54:55], v[54:55], v[122:123]
	v_mfma_f32_16x16x32_bf16 v[140:143], v[108:111], v[12:15], v[140:143]
	s_waitcnt lgkmcnt(5)
	v_pk_mul_f32 v[56:57], v[56:57], v[128:129]
	v_pk_mul_f32 v[58:59], v[58:59], v[130:131]
	ds_read_b128 v[68:71], v98 offset:4096
	ds_read_b128 v[72:75], v98 offset:4160
	ds_read_b128 v[76:79], v99 offset:18432
	ds_read_b128 v[80:83], v99 offset:18496
	ds_read_b128 v[84:87], v99 offset:18560
	s_waitcnt lgkmcnt(6)
	v_fma_f32 v144, v136, v140, v142
	v_fmac_f32_e32 v144, v137, v97
	v_cndmask_b32_e64 v145, v97, v144, s[10:11]
	v_cndmask_b32_e64 v145, v145, v140, s[8:9]
	v_fma_f32 v50, v138, v140, v143
	v_fmac_f32_e32 v50, v139, v97
	v_mfma_f32_16x16x4_f32 v[64:67], v132, v145, v[64:67]
	ds_read_b128 v[88:91], v99 offset:18624
	v_add_u32_e32 v0, 0x400, v0
	ds_read2_b32 v[92:93], v0 offset1:16
	ds_read2_b32 v[94:95], v0 offset0:32 offset1:48
	v_mfma_f32_16x16x4_f32 v[60:63], v133, v145, v[60:63]
	ds_read_b32 v96, v1 offset:4096
	ds_read_b128 v[100:103], v2 offset:128
	v_cndmask_b32_e64 v50, v50, v141, s[8:9]
	ds_write_b32 v3, v50 offset:3584
	v_mfma_f32_16x16x4_f32 v[52:55], v134, v145, v[52:55]
	v_cvt_pk_bf16_f32 v8, v64, v65
	v_cvt_pk_bf16_f32 v9, v66, v67
	v_mfma_f32_16x16x4_f32 v[56:59], v135, v145, v[56:59]
	s_waitcnt lgkmcnt(6)
	v_pk_mul_f32 v[64:65], v[64:65], v[76:77]
	v_pk_mul_f32 v[66:67], v[66:67], v[78:79]
	v_cvt_pk_bf16_f32 v10, v60, v61
	v_cvt_pk_bf16_f32 v11, v62, v63
	v_pk_mul_f32 v[60:61], v[60:61], v[80:81]
	v_pk_mul_f32 v[62:63], v[62:63], v[82:83]
	v_mfma_f32_16x16x32_bf16 v[140:143], v[68:71], v[8:11], 0
	v_cvt_pk_bf16_f32 v12, v52, v53
	v_cvt_pk_bf16_f32 v13, v54, v55
	v_cvt_pk_bf16_f32 v14, v56, v57
	v_cvt_pk_bf16_f32 v15, v58, v59
	v_pk_mul_f32 v[52:53], v[52:53], v[84:85]
	v_pk_mul_f32 v[54:55], v[54:55], v[86:87]
	v_mfma_f32_16x16x32_bf16 v[140:143], v[72:75], v[12:15], v[140:143]
	s_waitcnt lgkmcnt(5)
	v_pk_mul_f32 v[56:57], v[56:57], v[88:89]
	v_pk_mul_f32 v[58:59], v[58:59], v[90:91]
	ds_read_b128 v[104:107], v98 offset:4608
	ds_read_b128 v[108:111], v98 offset:4672
	ds_read_b128 v[112:115], v99 offset:18688
	ds_read_b128 v[116:119], v99 offset:18752
	ds_read_b128 v[120:123], v99 offset:18816
	s_waitcnt lgkmcnt(6)
; __device__ __forceinline__ void scan_head(const Params& p, LAS unsigned char* lds, int bh, const int wave) {
;     ...
;             bf16x8 Pa0, Pa1, Qa0, Qa1; f32x4 Pw0, Pw1, Pw2, Pw3, Qw0, Qw1, Qw2, Qw3, Pcs, Qcs; float Pb0, Pb1, Pb2, Pb3, Pvt, Pvu, Qb0, Qb1, Qb2, Qb3, Qvt, Qvu;
;             SCAN_LD(P, 0);
; #pragma unroll 1
;             for (int pi = 0; pi < 16; pi += 2) {
;                 SCAN_LD(Q, pi + 1);
;                 SCAN_STEP(P, pi);
;                 if (pi + 2 < 16) SCAN_LD(P, pi + 2);
;                 SCAN_STEP(Q, pi + 1);
;             }
	v_fma_f32 v144, v100, v140, v142
	v_fmac_f32_e32 v144, v101, v96
	v_cndmask_b32_e64 v145, v96, v144, s[10:11]
	v_cndmask_b32_e64 v145, v145, v140, s[8:9]
	v_fma_f32 v50, v102, v140, v143
	v_fmac_f32_e32 v50, v103, v96
	v_mfma_f32_16x16x4_f32 v[64:67], v92, v145, v[64:67]
	ds_read_b128 v[128:131], v99 offset:18880
	v_add_u32_e32 v0, 0x400, v0
	ds_read2_b32 v[132:133], v0 offset1:16
	ds_read2_b32 v[134:135], v0 offset0:32 offset1:48
	v_mfma_f32_16x16x4_f32 v[60:63], v93, v145, v[60:63]
	ds_read_b32 v97, v1 offset:4608
	ds_read_b128 v[136:139], v2 offset:144
	v_cndmask_b32_e64 v50, v50, v141, s[8:9]
	ds_write_b32 v3, v50 offset:4096
	v_mfma_f32_16x16x4_f32 v[52:55], v94, v145, v[52:55]
	v_cvt_pk_bf16_f32 v8, v64, v65
	v_cvt_pk_bf16_f32 v9, v66, v67
	v_mfma_f32_16x16x4_f32 v[56:59], v95, v145, v[56:59]
	s_waitcnt lgkmcnt(6)
	v_pk_mul_f32 v[64:65], v[64:65], v[112:113]
	v_pk_mul_f32 v[66:67], v[66:67], v[114:115]
	v_cvt_pk_bf16_f32 v10, v60, v61
	v_cvt_pk_bf16_f32 v11, v62, v63
	v_pk_mul_f32 v[60:61], v[60:61], v[116:117]
	v_pk_mul_f32 v[62:63], v[62:63], v[118:119]
	v_mfma_f32_16x16x32_bf16 v[140:143], v[104:107], v[8:11], 0
	v_cvt_pk_bf16_f32 v12, v52, v53
	v_cvt_pk_bf16_f32 v13, v54, v55
	v_cvt_pk_bf16_f32 v14, v56, v57
	v_cvt_pk_bf16_f32 v15, v58, v59
	v_pk_mul_f32 v[52:53], v[52:53], v[120:121]
	v_pk_mul_f32 v[54:55], v[54:55], v[122:123]
	v_mfma_f32_16x16x32_bf16 v[140:143], v[108:111], v[12:15], v[140:143]
	s_waitcnt lgkmcnt(5)
	v_pk_mul_f32 v[56:57], v[56:57], v[128:129]
	v_pk_mul_f32 v[58:59], v[58:59], v[130:131]
	ds_read_b128 v[68:71], v98 offset:5120
	ds_read_b128 v[72:75], v98 offset:5184
	ds_read_b128 v[76:79], v99 offset:18944
	ds_read_b128 v[80:83], v99 offset:19008
	ds_read_b128 v[84:87], v99 offset:19072
	s_waitcnt lgkmcnt(6)
	v_fma_f32 v144, v136, v140, v142
	v_fmac_f32_e32 v144, v137, v97
	v_cndmask_b32_e64 v145, v97, v144, s[10:11]
	v_cndmask_b32_e64 v145, v145, v140, s[8:9]
	v_fma_f32 v50, v138, v140, v143
	v_fmac_f32_e32 v50, v139, v97
	v_mfma_f32_16x16x4_f32 v[64:67], v132, v145, v[64:67]
	ds_read_b128 v[88:91], v99 offset:19136
	v_add_u32_e32 v0, 0x400, v0
	ds_read2_b32 v[92:93], v0 offset1:16
	ds_read2_b32 v[94:95], v0 offset0:32 offset1:48
	v_mfma_f32_16x16x4_f32 v[60:63], v133, v145, v[60:63]
	ds_read_b32 v96, v1 offset:5120
	ds_read_b128 v[100:103], v2 offset:160
	v_cndmask_b32_e64 v50, v50, v141, s[8:9]
	ds_write_b32 v3, v50 offset:4608
	v_mfma_f32_16x16x4_f32 v[52:55], v134, v145, v[52:55]
	v_cvt_pk_bf16_f32 v8, v64, v65
	v_cvt_pk_bf16_f32 v9, v66, v67
	v_mfma_f32_16x16x4_f32 v[56:59], v135, v145, v[56:59]
	s_waitcnt lgkmcnt(6)
	v_pk_mul_f32 v[64:65], v[64:65], v[76:77]
	v_pk_mul_f32 v[66:67], v[66:67], v[78:79]
	v_cvt_pk_bf16_f32 v10, v60, v61
	v_cvt_pk_bf16_f32 v11, v62, v63
	v_pk_mul_f32 v[60:61], v[60:61], v[80:81]
	v_pk_mul_f32 v[62:63], v[62:63], v[82:83]
	v_mfma_f32_16x16x32_bf16 v[140:143], v[68:71], v[8:11], 0
	v_cvt_pk_bf16_f32 v12, v52, v53
	v_cvt_pk_bf16_f32 v13, v54, v55
	v_cvt_pk_bf16_f32 v14, v56, v57
	v_cvt_pk_bf16_f32 v15, v58, v59
	v_pk_mul_f32 v[52:53], v[52:53], v[84:85]
	v_pk_mul_f32 v[54:55], v[54:55], v[86:87]
	v_mfma_f32_16x16x32_bf16 v[140:143], v[72:75], v[12:15], v[140:143]
	s_waitcnt lgkmcnt(5)
	v_pk_mul_f32 v[56:57], v[56:57], v[88:89]
	v_pk_mul_f32 v[58:59], v[58:59], v[90:91]
	ds_read_b128 v[104:107], v98 offset:5632
	ds_read_b128 v[108:111], v98 offset:5696
	ds_read_b128 v[112:115], v99 offset:19200
	ds_read_b128 v[116:119], v99 offset:19264
	ds_read_b128 v[120:123], v99 offset:19328
	s_waitcnt lgkmcnt(6)
	v_fma_f32 v144, v100, v140, v142
	v_fmac_f32_e32 v144, v101, v96
	v_cndmask_b32_e64 v145, v96, v144, s[10:11]
	v_cndmask_b32_e64 v145, v145, v140, s[8:9]
	v_fma_f32 v50, v102, v140, v143
	v_fmac_f32_e32 v50, v103, v96
	v_mfma_f32_16x16x4_f32 v[64:67], v92, v145, v[64:67]
	ds_read_b128 v[128:131], v99 offset:19392
	v_add_u32_e32 v0, 0x400, v0
	ds_read2_b32 v[132:133], v0 offset1:16
	ds_read2_b32 v[134:135], v0 offset0:32 offset1:48
	v_mfma_f32_16x16x4_f32 v[60:63], v93, v145, v[60:63]
	ds_read_b32 v97, v1 offset:5632
	ds_read_b128 v[136:139], v2 offset:176
	v_cndmask_b32_e64 v50, v50, v141, s[8:9]
	ds_write_b32 v3, v50 offset:5120
	v_mfma_f32_16x16x4_f32 v[52:55], v94, v145, v[52:55]
	v_cvt_pk_bf16_f32 v8, v64, v65
	v_cvt_pk_bf16_f32 v9, v66, v67
	v_mfma_f32_16x16x4_f32 v[56:59], v95, v145, v[56:59]
	s_waitcnt lgkmcnt(6)
	v_pk_mul_f32 v[64:65], v[64:65], v[112:113]
	v_pk_mul_f32 v[66:67], v[66:67], v[114:115]
	v_cvt_pk_bf16_f32 v10, v60, v61
	v_cvt_pk_bf16_f32 v11, v62, v63
	v_pk_mul_f32 v[60:61], v[60:61], v[116:117]
	v_pk_mul_f32 v[62:63], v[62:63], v[118:119]
	v_mfma_f32_16x16x32_bf16 v[140:143], v[104:107], v[8:11], 0
	v_cvt_pk_bf16_f32 v12, v52, v53
	v_cvt_pk_bf16_f32 v13, v54, v55
	v_cvt_pk_bf16_f32 v14, v56, v57
	v_cvt_pk_bf16_f32 v15, v58, v59
	v_pk_mul_f32 v[52:53], v[52:53], v[120:121]
	v_pk_mul_f32 v[54:55], v[54:55], v[122:123]
	v_mfma_f32_16x16x32_bf16 v[140:143], v[108:111], v[12:15], v[140:143]
	s_waitcnt lgkmcnt(5)
	v_pk_mul_f32 v[56:57], v[56:57], v[128:129]
	v_pk_mul_f32 v[58:59], v[58:59], v[130:131]
	ds_read_b128 v[68:71], v98 offset:6144
	ds_read_b128 v[72:75], v98 offset:6208
	ds_read_b128 v[76:79], v99 offset:19456
	ds_read_b128 v[80:83], v99 offset:19520
	ds_read_b128 v[84:87], v99 offset:19584
	s_waitcnt lgkmcnt(6)
; __device__ __forceinline__ void scan_head(const Params& p, LAS unsigned char* lds, int bh, const int wave) {
;     ...
;             bf16x8 Pa0, Pa1, Qa0, Qa1; f32x4 Pw0, Pw1, Pw2, Pw3, Qw0, Qw1, Qw2, Qw3, Pcs, Qcs; float Pb0, Pb1, Pb2, Pb3, Pvt, Pvu, Qb0, Qb1, Qb2, Qb3, Qvt, Qvu;
;             SCAN_LD(P, 0);
; #pragma unroll 1
;             for (int pi = 0; pi < 16; pi += 2) {
;                 SCAN_LD(Q, pi + 1);
;                 SCAN_STEP(P, pi);
;                 if (pi + 2 < 16) SCAN_LD(P, pi + 2);
;                 SCAN_STEP(Q, pi + 1);
;             }
	v_fma_f32 v144, v136, v140, v142
	v_fmac_f32_e32 v144, v137, v97
	v_cndmask_b32_e64 v145, v97, v144, s[10:11]
	v_cndmask_b32_e64 v145, v145, v140, s[8:9]
	v_fma_f32 v50, v138, v140, v143
	v_fmac_f32_e32 v50, v139, v97
	v_mfma_f32_16x16x4_f32 v[64:67], v132, v145, v[64:67]
	ds_read_b128 v[88:91], v99 offset:19648
	v_add_u32_e32 v0, 0x400, v0
	ds_read2_b32 v[92:93], v0 offset1:16
	ds_read2_b32 v[94:95], v0 offset0:32 offset1:48
	v_mfma_f32_16x16x4_f32 v[60:63], v133, v145, v[60:63]
	ds_read_b32 v96, v1 offset:6144
	ds_read_b128 v[100:103], v2 offset:192
	v_cndmask_b32_e64 v50, v50, v141, s[8:9]
	ds_write_b32 v3, v50 offset:5632
	v_mfma_f32_16x16x4_f32 v[52:55], v134, v145, v[52:55]
	v_cvt_pk_bf16_f32 v8, v64, v65
	v_cvt_pk_bf16_f32 v9, v66, v67
	v_mfma_f32_16x16x4_f32 v[56:59], v135, v145, v[56:59]
	s_waitcnt lgkmcnt(6)
	v_pk_mul_f32 v[64:65], v[64:65], v[76:77]
	v_pk_mul_f32 v[66:67], v[66:67], v[78:79]
	v_cvt_pk_bf16_f32 v10, v60, v61
	v_cvt_pk_bf16_f32 v11, v62, v63
	v_pk_mul_f32 v[60:61], v[60:61], v[80:81]
	v_pk_mul_f32 v[62:63], v[62:63], v[82:83]
	v_mfma_f32_16x16x32_bf16 v[140:143], v[68:71], v[8:11], 0
	v_cvt_pk_bf16_f32 v12, v52, v53
	v_cvt_pk_bf16_f32 v13, v54, v55
	v_cvt_pk_bf16_f32 v14, v56, v57
	v_cvt_pk_bf16_f32 v15, v58, v59
	v_pk_mul_f32 v[52:53], v[52:53], v[84:85]
	v_pk_mul_f32 v[54:55], v[54:55], v[86:87]
	v_mfma_f32_16x16x32_bf16 v[140:143], v[72:75], v[12:15], v[140:143]
	s_waitcnt lgkmcnt(5)
	v_pk_mul_f32 v[56:57], v[56:57], v[88:89]
	v_pk_mul_f32 v[58:59], v[58:59], v[90:91]
	ds_read_b128 v[104:107], v98 offset:6656
	ds_read_b128 v[108:111], v98 offset:6720
	ds_read_b128 v[112:115], v99 offset:19712
	ds_read_b128 v[116:119], v99 offset:19776
	ds_read_b128 v[120:123], v99 offset:19840
	s_waitcnt lgkmcnt(6)
	v_fma_f32 v144, v100, v140, v142
	v_fmac_f32_e32 v144, v101, v96
	v_cndmask_b32_e64 v145, v96, v144, s[10:11]
	v_cndmask_b32_e64 v145, v145, v140, s[8:9]
	v_fma_f32 v50, v102, v140, v143
	v_fmac_f32_e32 v50, v103, v96
	v_mfma_f32_16x16x4_f32 v[64:67], v92, v145, v[64:67]
	ds_read_b128 v[128:131], v99 offset:19904
	v_add_u32_e32 v0, 0x400, v0
	ds_read2_b32 v[132:133], v0 offset1:16
	ds_read2_b32 v[134:135], v0 offset0:32 offset1:48
	v_mfma_f32_16x16x4_f32 v[60:63], v93, v145, v[60:63]
	ds_read_b32 v97, v1 offset:6656
	ds_read_b128 v[136:139], v2 offset:208
	v_cndmask_b32_e64 v50, v50, v141, s[8:9]
	ds_write_b32 v3, v50 offset:6144
	v_mfma_f32_16x16x4_f32 v[52:55], v94, v145, v[52:55]
	v_cvt_pk_bf16_f32 v8, v64, v65
	v_cvt_pk_bf16_f32 v9, v66, v67
	v_mfma_f32_16x16x4_f32 v[56:59], v95, v145, v[56:59]
	s_waitcnt lgkmcnt(6)
	v_pk_mul_f32 v[64:65], v[64:65], v[112:113]
	v_pk_mul_f32 v[66:67], v[66:67], v[114:115]
	v_cvt_pk_bf16_f32 v10, v60, v61
	v_cvt_pk_bf16_f32 v11, v62, v63
	v_pk_mul_f32 v[60:61], v[60:61], v[116:117]
	v_pk_mul_f32 v[62:63], v[62:63], v[118:119]
	v_mfma_f32_16x16x32_bf16 v[140:143], v[104:107], v[8:11], 0
	v_cvt_pk_bf16_f32 v12, v52, v53
	v_cvt_pk_bf16_f32 v13, v54, v55
	v_cvt_pk_bf16_f32 v14, v56, v57
	v_cvt_pk_bf16_f32 v15, v58, v59
	v_pk_mul_f32 v[52:53], v[52:53], v[120:121]
	v_pk_mul_f32 v[54:55], v[54:55], v[122:123]
	v_mfma_f32_16x16x32_bf16 v[140:143], v[108:111], v[12:15], v[140:143]
	s_waitcnt lgkmcnt(5)
	v_pk_mul_f32 v[56:57], v[56:57], v[128:129]
	v_pk_mul_f32 v[58:59], v[58:59], v[130:131]
	ds_read_b128 v[68:71], v98 offset:7168
	ds_read_b128 v[72:75], v98 offset:7232
	ds_read_b128 v[76:79], v99 offset:19968
	ds_read_b128 v[80:83], v99 offset:20032
	ds_read_b128 v[84:87], v99 offset:20096
	s_waitcnt lgkmcnt(6)
; __device__ __forceinline__ void scan_head(const Params& p, LAS unsigned char* lds, int bh, const int wave) {
;     ...
;             bf16x8 Pa0, Pa1, Qa0, Qa1; f32x4 Pw0, Pw1, Pw2, Pw3, Qw0, Qw1, Qw2, Qw3, Pcs, Qcs; float Pb0, Pb1, Pb2, Pb3, Pvt, Pvu, Qb0, Qb1, Qb2, Qb3, Qvt, Qvu;
;             SCAN_LD(P, 0);
; #pragma unroll 1
;             for (int pi = 0; pi < 16; pi += 2) {
;                 SCAN_LD(Q, pi + 1);
;                 SCAN_STEP(P, pi);
;                 if (pi + 2 < 16) SCAN_LD(P, pi + 2);
;                 SCAN_STEP(Q, pi + 1);
;             }
	v_fma_f32 v144, v136, v140, v142
	v_fmac_f32_e32 v144, v137, v97
	v_cndmask_b32_e64 v145, v97, v144, s[10:11]
	v_cndmask_b32_e64 v145, v145, v140, s[8:9]
	v_fma_f32 v50, v138, v140, v143
	v_fmac_f32_e32 v50, v139, v97
	v_mfma_f32_16x16x4_f32 v[64:67], v132, v145, v[64:67]
	ds_read_b128 v[88:91], v99 offset:20160
	v_add_u32_e32 v0, 0x400, v0
	ds_read2_b32 v[92:93], v0 offset1:16
	ds_read2_b32 v[94:95], v0 offset0:32 offset1:48
	v_mfma_f32_16x16x4_f32 v[60:63], v133, v145, v[60:63]
	ds_read_b32 v96, v1 offset:7168
	ds_read_b128 v[100:103], v2 offset:224
	v_cndmask_b32_e64 v50, v50, v141, s[8:9]
	ds_write_b32 v3, v50 offset:6656
	v_mfma_f32_16x16x4_f32 v[52:55], v134, v145, v[52:55]
	v_cvt_pk_bf16_f32 v8, v64, v65
	v_cvt_pk_bf16_f32 v9, v66, v67
	v_mfma_f32_16x16x4_f32 v[56:59], v135, v145, v[56:59]
	s_waitcnt lgkmcnt(6)
	v_pk_mul_f32 v[64:65], v[64:65], v[76:77]
	v_pk_mul_f32 v[66:67], v[66:67], v[78:79]
	v_cvt_pk_bf16_f32 v10, v60, v61
	v_cvt_pk_bf16_f32 v11, v62, v63
	v_pk_mul_f32 v[60:61], v[60:61], v[80:81]
	v_pk_mul_f32 v[62:63], v[62:63], v[82:83]
	v_mfma_f32_16x16x32_bf16 v[140:143], v[68:71], v[8:11], 0
	v_cvt_pk_bf16_f32 v12, v52, v53
	v_cvt_pk_bf16_f32 v13, v54, v55
	v_cvt_pk_bf16_f32 v14, v56, v57
	v_cvt_pk_bf16_f32 v15, v58, v59
	v_pk_mul_f32 v[52:53], v[52:53], v[84:85]
	v_pk_mul_f32 v[54:55], v[54:55], v[86:87]
	v_mfma_f32_16x16x32_bf16 v[140:143], v[72:75], v[12:15], v[140:143]
	s_waitcnt lgkmcnt(5)
	v_pk_mul_f32 v[56:57], v[56:57], v[88:89]
	v_pk_mul_f32 v[58:59], v[58:59], v[90:91]
	ds_read_b128 v[104:107], v98 offset:7680
	ds_read_b128 v[108:111], v98 offset:7744
	ds_read_b128 v[112:115], v99 offset:20224
	ds_read_b128 v[116:119], v99 offset:20288
	ds_read_b128 v[120:123], v99 offset:20352
	s_waitcnt lgkmcnt(6)
	v_fma_f32 v144, v100, v140, v142
	v_fmac_f32_e32 v144, v101, v96
	v_cndmask_b32_e64 v145, v96, v144, s[10:11]
	v_cndmask_b32_e64 v145, v145, v140, s[8:9]
	v_fma_f32 v50, v102, v140, v143
	v_fmac_f32_e32 v50, v103, v96
	v_mfma_f32_16x16x4_f32 v[64:67], v92, v145, v[64:67]
	ds_read_b128 v[128:131], v99 offset:20416
	v_add_u32_e32 v0, 0x400, v0
	ds_read2_b32 v[132:133], v0 offset1:16
	ds_read2_b32 v[134:135], v0 offset0:32 offset1:48
	v_mfma_f32_16x16x4_f32 v[60:63], v93, v145, v[60:63]
	ds_read_b32 v97, v1 offset:7680
	ds_read_b128 v[136:139], v2 offset:240
	v_cndmask_b32_e64 v50, v50, v141, s[8:9]
	ds_write_b32 v3, v50 offset:7168
	v_mfma_f32_16x16x4_f32 v[52:55], v94, v145, v[52:55]
	v_cvt_pk_bf16_f32 v8, v64, v65
	v_cvt_pk_bf16_f32 v9, v66, v67
	v_mfma_f32_16x16x4_f32 v[56:59], v95, v145, v[56:59]
	s_waitcnt lgkmcnt(6)
	v_pk_mul_f32 v[64:65], v[64:65], v[112:113]
	v_pk_mul_f32 v[66:67], v[66:67], v[114:115]
	v_cvt_pk_bf16_f32 v10, v60, v61
	v_cvt_pk_bf16_f32 v11, v62, v63
	v_pk_mul_f32 v[60:61], v[60:61], v[116:117]
	v_pk_mul_f32 v[62:63], v[62:63], v[118:119]
	v_mfma_f32_16x16x32_bf16 v[140:143], v[104:107], v[8:11], 0
	v_cvt_pk_bf16_f32 v12, v52, v53
	v_cvt_pk_bf16_f32 v13, v54, v55
	v_cvt_pk_bf16_f32 v14, v56, v57
	v_cvt_pk_bf16_f32 v15, v58, v59
	v_pk_mul_f32 v[52:53], v[52:53], v[120:121]
	v_pk_mul_f32 v[54:55], v[54:55], v[122:123]
	v_mfma_f32_16x16x32_bf16 v[140:143], v[108:111], v[12:15], v[140:143]
	s_waitcnt lgkmcnt(5)
	v_pk_mul_f32 v[56:57], v[56:57], v[128:129]
	v_pk_mul_f32 v[58:59], v[58:59], v[130:131]
	s_waitcnt lgkmcnt(1)
	s_nop 3
	v_fma_f32 v144, v136, v140, v142
	v_fmac_f32_e32 v144, v137, v97
	v_cndmask_b32_e64 v145, v97, v144, s[10:11]
	v_cndmask_b32_e64 v145, v145, v140, s[8:9]
	v_fma_f32 v50, v138, v140, v143
	v_fmac_f32_e32 v50, v139, v97
	v_mfma_f32_16x16x4_f32 v[64:67], v132, v145, v[64:67]
	v_cndmask_b32_e64 v50, v50, v141, s[8:9]
	ds_write_b32 v3, v50 offset:7680
	v_mfma_f32_16x16x4_f32 v[60:63], v133, v145, v[60:63]
	v_mfma_f32_16x16x4_f32 v[52:55], v134, v145, v[52:55]
	v_mfma_f32_16x16x4_f32 v[56:59], v135, v145, v[56:59]
	s_waitcnt lgkmcnt(0)
	s_nop 7
	s_nop 3
